# wconv tile 64(k)x128(n): 16 KB LDS, 54 VGPRs, 8 workgroups per CU
# speedup vs baseline: 1.0170x; 1.0022x over previous
_Z12wconv_kernel5WDesci:
	s_movk_i32 s5, 0x800
	s_cmp_lt_u32 s3, 5
	s_cselect_b32 s4, 0x200, s5
	s_cmp_ge_u32 s2, s4
	s_cbranch_scc1 .Lwc_exit
	s_mov_b32 s4, s2
	s_load_dword s8, s[0:1], 0x150
	s_cmp_eq_u32 s3, 5
	s_cselect_b32 s9, 13, 11
	s_cmp_eq_u32 s3, 6
	s_cselect_b32 s10, 13, 11
	s_sub_u32 s11, s9, 7
	s_lshr_b32 s12, s4, s11
	s_lshl_b32 s13, s12, s11
	s_sub_u32 s13, s4, s13
	s_add_u32 s20, s9, 2
	s_add_u32 s21, s10, 1
	v_lshrrev_b32_e32 v4, 5, v0
	v_and_b32_e32 v6, 31, v0
	v_lshlrev_b32_e32 v5, 3, v4
	v_lshlrev_b32_e32 v5, s20, v5
	v_lshl_add_u32 v1, v6, 4, v5
	v_and_b32_e32 v8, 7, v6
	v_xor_b32_e32 v7, v4, v8
	v_lshlrev_b32_e32 v7, 4, v7
	v_lshl_add_u32 v2, v6, 9, v7
	v_lshrrev_b32_e32 v9, 3, v0
	v_and_b32_e32 v10, 7, v0
	v_xor_b32_e32 v11, v10, v4
	v_lshlrev_b32_e32 v11, 4, v11
	v_lshl_add_u32 v52, v9, 7, v11
	v_lshlrev_b32_e32 v12, s21, v9
	v_lshl_add_u32 v53, v10, 4, v12
	s_add_u32 s22, s20, 6
	s_lshl_b32 s23, s12, s22
	s_lshl_b32 s24, s13, 9
	s_add_u32 s23, s23, s24
	s_lshl_b32 s25, 1, s20
	s_add_u32 s26, s21, 7
	s_lshl_b32 s27, s13, s26
	s_lshl_b32 s28, s12, 7
	s_add_u32 s27, s27, s28
	s_add_u32 s29, s10, 6
	s_lshl_b32 s29, 1, s29
	s_waitcnt lgkmcnt(0)
	s_add_u32 s8, s8, s3
	s_lshl_b32 s8, s8, 3
	s_add_u32 s14, s0, s8
	s_addc_u32 s15, s1, 0
	s_load_dwordx2 s[16:17], s[14:15], 0x0
	s_load_dwordx2 s[18:19], s[14:15], 0x70
	s_waitcnt lgkmcnt(0)
	s_add_u32 s16, s16, s23
	s_addc_u32 s17, s17, 0
	s_add_u32 s18, s18, s27
	s_addc_u32 s19, s19, 0
	global_load_dwordx4 v[4:7], v1, s[16:17] sc1 nt
	s_add_u32 s16, s16, s25
	s_addc_u32 s17, s17, 0
	global_load_dwordx4 v[8:11], v1, s[16:17] sc1 nt
	s_add_u32 s16, s16, s25
	s_addc_u32 s17, s17, 0
	global_load_dwordx4 v[12:15], v1, s[16:17] sc1 nt
	s_add_u32 s16, s16, s25
	s_addc_u32 s17, s17, 0
	global_load_dwordx4 v[16:19], v1, s[16:17] sc1 nt
	s_add_u32 s16, s16, s25
	s_addc_u32 s17, s17, 0
	global_load_dwordx4 v[20:23], v1, s[16:17] sc1 nt
	s_add_u32 s16, s16, s25
	s_addc_u32 s17, s17, 0
	global_load_dwordx4 v[24:27], v1, s[16:17] sc1 nt
	s_add_u32 s16, s16, s25
	s_addc_u32 s17, s17, 0
	global_load_dwordx4 v[28:31], v1, s[16:17] sc1 nt
	s_add_u32 s16, s16, s25
	s_addc_u32 s17, s17, 0
	global_load_dwordx4 v[32:35], v1, s[16:17] sc1 nt
	s_waitcnt vmcnt(6)
	v_cvt_pk_f16_f32 v36, v4, v8
	v_cvt_pk_f16_f32 v40, v5, v9
	v_cvt_pk_f16_f32 v44, v6, v10
	v_cvt_pk_f16_f32 v48, v7, v11
	s_waitcnt vmcnt(4)
	v_cvt_pk_f16_f32 v37, v12, v16
	v_cvt_pk_f16_f32 v41, v13, v17
	v_cvt_pk_f16_f32 v45, v14, v18
	v_cvt_pk_f16_f32 v49, v15, v19
	s_waitcnt vmcnt(2)
	v_cvt_pk_f16_f32 v38, v20, v24
	v_cvt_pk_f16_f32 v42, v21, v25
	v_cvt_pk_f16_f32 v46, v22, v26
	v_cvt_pk_f16_f32 v50, v23, v27
	s_waitcnt vmcnt(0)
	v_cvt_pk_f16_f32 v39, v28, v32
	v_cvt_pk_f16_f32 v43, v29, v33
	v_cvt_pk_f16_f32 v47, v30, v34
	v_cvt_pk_f16_f32 v51, v31, v35
	ds_write_b128 v2, v[36:39]
	ds_write_b128 v2, v[40:43] offset:128
	ds_write_b128 v2, v[44:47] offset:256
	ds_write_b128 v2, v[48:51] offset:384
	s_waitcnt lgkmcnt(0)
	s_barrier
	ds_read_b128 v[4:7], v52
	ds_read_b128 v[8:11], v52 offset:4096
	ds_read_b128 v[12:15], v52 offset:8192
	ds_read_b128 v[16:19], v52 offset:12288
	s_waitcnt lgkmcnt(3)
	global_store_dwordx4 v53, v[4:7], s[18:19] sc1
	s_add_u32 s18, s18, s29
	s_addc_u32 s19, s19, 0
	s_waitcnt lgkmcnt(2)
	global_store_dwordx4 v53, v[8:11], s[18:19] sc1
	s_add_u32 s18, s18, s29
	s_addc_u32 s19, s19, 0
	s_waitcnt lgkmcnt(1)
	global_store_dwordx4 v53, v[12:15], s[18:19] sc1
	s_add_u32 s18, s18, s29
	s_addc_u32 s19, s19, 0
	s_waitcnt lgkmcnt(0)
	global_store_dwordx4 v53, v[16:19], s[18:19] sc1

	.amdhsa_kernel _Z12wconv_kernel5WDesci
		.amdhsa_group_segment_fixed_size 16640
		.amdhsa_private_segment_fixed_size 0
		.amdhsa_kernarg_size 340
		.amdhsa_user_sgpr_count 2
		.amdhsa_user_sgpr_dispatch_ptr 0
		.amdhsa_user_sgpr_queue_ptr 0
		.amdhsa_user_sgpr_kernarg_segment_ptr 1
		.amdhsa_user_sgpr_dispatch_id 0
		.amdhsa_user_sgpr_kernarg_preload_length 0
		.amdhsa_user_sgpr_kernarg_preload_offset 0
		.amdhsa_user_sgpr_private_segment_size 0
		.amdhsa_uses_dynamic_stack 0
		.amdhsa_enable_private_segment 0
		.amdhsa_system_sgpr_workgroup_id_x 1
		.amdhsa_system_sgpr_workgroup_id_y 1
		.amdhsa_system_sgpr_workgroup_id_z 0
		.amdhsa_system_sgpr_workgroup_info 0
		.amdhsa_system_vgpr_workitem_id 0
		.amdhsa_next_free_vgpr 54
		.amdhsa_next_free_sgpr 30
		.amdhsa_accum_offset 56
		.amdhsa_reserve_vcc 0
		.amdhsa_float_round_mode_32 0
		.amdhsa_float_round_mode_16_64 0
		.amdhsa_float_denorm_mode_32 3
		.amdhsa_float_denorm_mode_16_64 3
		.amdhsa_dx10_clamp 1
		.amdhsa_ieee_mode 1
		.amdhsa_fp16_overflow 0
		.amdhsa_tg_split 0
		.amdhsa_exception_fp_ieee_invalid_op 0
		.amdhsa_exception_fp_denorm_src 0
		.amdhsa_exception_fp_ieee_div_zero 0
		.amdhsa_exception_fp_ieee_overflow 0
		.amdhsa_exception_fp_ieee_underflow 0
		.amdhsa_exception_fp_ieee_inexact 0
		.amdhsa_exception_int_div_zero 0
	.end_amdhsa_kernel

amdhsa.kernels:
  - .agpr_count:     0
    .args:
      - .offset:         0
        .size:           336
        .value_kind:     by_value
      - .offset:         336
        .size:           4
        .value_kind:     by_value
    .group_segment_fixed_size: 16640
    .kernarg_segment_align: 8
    .kernarg_segment_size: 340
    .language:       OpenCL C
    .language_version:
      - 2
      - 0
    .max_flat_workgroup_size: 256
    .name:           _Z12wconv_kernel5WDesci
    .private_segment_fixed_size: 0
    .sgpr_count:     36
    .sgpr_spill_count: 0
    .symbol:         _Z12wconv_kernel5WDesci.kd
    .uniform_work_group_size: 1
    .uses_dynamic_stack: false
    .vgpr_count:     54
    .vgpr_spill_count: 0
    .wavefront_size: 64
  - .agpr_count:     128
    .args:
      - .actual_access:  read_only
        .address_space:  global
        .offset:         0
        .size:           8
        .value_kind:     global_buffer
      - .address_space:  global
        .offset:         8
        .size:           8
        .value_kind:     global_buffer
      - .address_space:  global
        .offset:         16
        .size:           8
        .value_kind:     global_buffer
      - .actual_access:  read_only
        .address_space:  global
        .offset:         24
        .size:           8
        .value_kind:     global_buffer
      - .actual_access:  read_only
        .address_space:  global
        .offset:         32
        .size:           8
        .value_kind:     global_buffer
      - .actual_access:  read_only
        .address_space:  global
        .offset:         40
        .size:           8
        .value_kind:     global_buffer
      - .actual_access:  write_only
        .address_space:  global
        .offset:         48
        .size:           8
        .value_kind:     global_buffer
    .group_segment_fixed_size: 0
    .kernarg_segment_align: 8
    .kernarg_segment_size: 56
    .language:       OpenCL C
    .language_version:
      - 2
      - 0
    .max_flat_workgroup_size: 256
    .name:           _Z8ret_fastPKtS0_S0_S0_PKfS2_Pt
    .private_segment_fixed_size: 0
    .sgpr_count:     85
    .sgpr_spill_count: 0
    .symbol:         _Z8ret_fastPKtS0_S0_S0_PKfS2_Pt.kd
    .uniform_work_group_size: 1
    .uses_dynamic_stack: false
    .vgpr_count:     348
    .vgpr_spill_count: 0
    .wavefront_size: 64
  - .agpr_count:     0
    .args:
      - .actual_access:  read_only
        .address_space:  global
        .offset:         0
        .size:           8
        .value_kind:     global_buffer
      - .actual_access:  read_only
        .address_space:  global
        .offset:         8
        .size:           8
        .value_kind:     global_buffer
      - .actual_access:  read_only
        .address_space:  global
        .offset:         16
        .size:           8
        .value_kind:     global_buffer
      - .actual_access:  read_only
        .address_space:  global
        .offset:         24
        .size:           8
        .value_kind:     global_buffer
      - .actual_access:  write_only
        .address_space:  global
        .offset:         32
        .size:           8
        .value_kind:     global_buffer
      - .actual_access:  write_only
        .address_space:  global
        .offset:         40
        .size:           8
        .value_kind:     global_buffer
      - .actual_access:  read_only
        .address_space:  global
        .offset:         48
        .size:           8
        .value_kind:     global_buffer
      - .actual_access:  read_only
        .address_space:  global
        .offset:         56
        .size:           8
        .value_kind:     global_buffer
    .group_segment_fixed_size: 16
    .kernarg_segment_align: 8
    .kernarg_segment_size: 64
    .language:       OpenCL C
    .language_version:
      - 2
      - 0
    .max_flat_workgroup_size: 256
    .name:           _Z9ln_kernelILb0ELb0EEvPKvPKtS3_PKfPvPtS5_S5_
    .private_segment_fixed_size: 0
    .sgpr_count:     34
    .sgpr_spill_count: 0
    .symbol:         _Z9ln_kernelILb0ELb0EEvPKvPKtS3_PKfPvPtS5_S5_.kd
    .uniform_work_group_size: 1
    .uses_dynamic_stack: false
    .vgpr_count:     62
    .vgpr_spill_count: 0
    .wavefront_size: 64
  - .agpr_count:     0
    .args:
      - .actual_access:  read_only
        .address_space:  global
        .offset:         0
        .size:           8
        .value_kind:     global_buffer
      - .actual_access:  read_only
        .address_space:  global
        .offset:         8
        .size:           8
        .value_kind:     global_buffer
      - .actual_access:  read_only
        .address_space:  global
        .offset:         16
        .size:           8
        .value_kind:     global_buffer
      - .actual_access:  read_only
        .address_space:  global
        .offset:         24
        .size:           8
        .value_kind:     global_buffer
      - .actual_access:  write_only
        .address_space:  global
        .offset:         32
        .size:           8
        .value_kind:     global_buffer
      - .actual_access:  write_only
        .address_space:  global
        .offset:         40
        .size:           8
        .value_kind:     global_buffer
      - .actual_access:  read_only
        .address_space:  global
        .offset:         48
        .size:           8
        .value_kind:     global_buffer
      - .actual_access:  read_only
        .address_space:  global
        .offset:         56
        .size:           8
        .value_kind:     global_buffer
    .group_segment_fixed_size: 16
    .kernarg_segment_align: 8
    .kernarg_segment_size: 64
    .language:       OpenCL C
    .language_version:
      - 2
      - 0
    .max_flat_workgroup_size: 256
    .name:           _Z9ln_kernelILb1ELb1EEvPKvPKtS3_PKfPvPtS5_S5_
    .private_segment_fixed_size: 0
    .sgpr_count:     34
    .sgpr_spill_count: 0
    .symbol:         _Z9ln_kernelILb1ELb1EEvPKvPKtS3_PKfPvPtS5_S5_.kd
    .uniform_work_group_size: 1
    .uses_dynamic_stack: false
    .vgpr_count:     62
    .vgpr_spill_count: 0
    .wavefront_size: 64
  - .agpr_count:     0
    .args:
      - .address_space:  global
        .offset:         0
        .size:           8
        .value_kind:     global_buffer
      - .address_space:  global
        .offset:         8
        .size:           8
        .value_kind:     global_buffer
      - .offset:         16
        .size:           4
        .value_kind:     by_value
      - .offset:         20
        .size:           4
        .value_kind:     by_value
      - .offset:         24
        .size:           4
        .value_kind:     by_value
      - .offset:         28
        .size:           4
        .value_kind:     by_value
      - .offset:         32
        .size:           40
        .value_kind:     by_value
      - .offset:         72
        .size:           4
        .value_kind:     hidden_block_count_x
      - .offset:         76
        .size:           4
        .value_kind:     hidden_block_count_y
      - .offset:         80
        .size:           4
        .value_kind:     hidden_block_count_z
      - .offset:         84
        .size:           2
        .value_kind:     hidden_group_size_x
      - .offset:         86
        .size:           2
        .value_kind:     hidden_group_size_y
      - .offset:         88
        .size:           2
        .value_kind:     hidden_group_size_z
      - .offset:         90
        .size:           2
        .value_kind:     hidden_remainder_x
      - .offset:         92
        .size:           2
        .value_kind:     hidden_remainder_y
      - .offset:         94
        .size:           2
        .value_kind:     hidden_remainder_z
      - .offset:         112
        .size:           8
        .value_kind:     hidden_global_offset_x
      - .offset:         120
        .size:           8
        .value_kind:     hidden_global_offset_y
      - .offset:         128
        .size:           8
        .value_kind:     hidden_global_offset_z
      - .offset:         136
        .size:           2
        .value_kind:     hidden_grid_dims
      - .offset:         192
        .size:           4
        .value_kind:     hidden_dynamic_lds_size
    .group_segment_fixed_size: 0
    .kernarg_segment_align: 8
    .kernarg_segment_size: 328
    .language:       OpenCL C
    .language_version:
      - 2
      - 0
    .max_flat_workgroup_size: 512
    .name:           _Z9gemm_fastILi0ELi2EEvPKtS1_iiii7EpiArgs
    .private_segment_fixed_size: 0
    .sgpr_count:     55
    .sgpr_spill_count: 0
    .symbol:         _Z9gemm_fastILi0ELi2EEvPKtS1_iiii7EpiArgs.kd
    .uniform_work_group_size: 1
    .uses_dynamic_stack: false
    .vgpr_count:     255
    .vgpr_spill_count: 0
    .wavefront_size: 64
  - .agpr_count:     0
    .args:
      - .address_space:  global
        .offset:         0
        .size:           8
        .value_kind:     global_buffer
      - .address_space:  global
        .offset:         8
        .size:           8
        .value_kind:     global_buffer
      - .offset:         16
        .size:           4
        .value_kind:     by_value
      - .offset:         20
        .size:           4
        .value_kind:     by_value
      - .offset:         24
        .size:           4
        .value_kind:     by_value
      - .offset:         28
        .size:           4
        .value_kind:     by_value
      - .offset:         32
        .size:           40
        .value_kind:     by_value
    .group_segment_fixed_size: 0
    .kernarg_segment_align: 8
    .kernarg_segment_size: 72
    .language:       OpenCL C
    .language_version:
      - 2
      - 0
    .max_flat_workgroup_size: 512
    .name:           _Z9gemm_fastILi1ELi1EEvPKtS1_iiii7EpiArgs
    .private_segment_fixed_size: 0
    .sgpr_count:     32
    .sgpr_spill_count: 0
    .symbol:         _Z9gemm_fastILi1ELi1EEvPKtS1_iiii7EpiArgs.kd
    .uniform_work_group_size: 1
    .uses_dynamic_stack: false
    .vgpr_count:     247
    .vgpr_spill_count: 0
    .wavefront_size: 64
  - .agpr_count:     0
    .args:
      - .actual_access:  read_only
        .address_space:  global
        .offset:         0
        .size:           8
        .value_kind:     global_buffer
      - .actual_access:  read_only
        .address_space:  global
        .offset:         8
        .size:           8
        .value_kind:     global_buffer
      - .actual_access:  read_only
        .address_space:  global
        .offset:         16
        .size:           8
        .value_kind:     global_buffer
      - .actual_access:  read_only
        .address_space:  global
        .offset:         24
        .size:           8
        .value_kind:     global_buffer
      - .actual_access:  write_only
        .address_space:  global
        .offset:         32
        .size:           8
        .value_kind:     global_buffer
      - .actual_access:  write_only
        .address_space:  global
        .offset:         40
        .size:           8
        .value_kind:     global_buffer
      - .actual_access:  read_only
        .address_space:  global
        .offset:         48
        .size:           8
        .value_kind:     global_buffer
      - .actual_access:  read_only
        .address_space:  global
        .offset:         56
        .size:           8
        .value_kind:     global_buffer
    .group_segment_fixed_size: 16
    .kernarg_segment_align: 8
    .kernarg_segment_size: 64
    .language:       OpenCL C
    .language_version:
      - 2
      - 0
    .max_flat_workgroup_size: 256
    .name:           _Z9ln_kernelILb0ELb1EEvPKvPKtS3_PKfPvPtS5_S5_
    .private_segment_fixed_size: 0
    .sgpr_count:     34
    .sgpr_spill_count: 0
    .symbol:         _Z9ln_kernelILb0ELb1EEvPKvPKtS3_PKfPvPtS5_S5_.kd
    .uniform_work_group_size: 1
    .uses_dynamic_stack: false
    .vgpr_count:     62
    .vgpr_spill_count: 0
    .wavefront_size: 64
  - .agpr_count:     0
    .args:
      - .address_space:  global
        .offset:         0
        .size:           8
        .value_kind:     global_buffer
      - .address_space:  global
        .offset:         8
        .size:           8
        .value_kind:     global_buffer
      - .offset:         16
        .size:           4
        .value_kind:     by_value
      - .offset:         20
        .size:           4
        .value_kind:     by_value
      - .offset:         24
        .size:           4
        .value_kind:     by_value
      - .offset:         28
        .size:           4
        .value_kind:     by_value
      - .offset:         32
        .size:           40
        .value_kind:     by_value
      - .offset:         72
        .size:           4
        .value_kind:     hidden_block_count_x
      - .offset:         76
        .size:           4
        .value_kind:     hidden_block_count_y
      - .offset:         80
        .size:           4
        .value_kind:     hidden_block_count_z
      - .offset:         84
        .size:           2
        .value_kind:     hidden_group_size_x
      - .offset:         86
        .size:           2
        .value_kind:     hidden_group_size_y
      - .offset:         88
        .size:           2
        .value_kind:     hidden_group_size_z
      - .offset:         90
        .size:           2
        .value_kind:     hidden_remainder_x
      - .offset:         92
        .size:           2
        .value_kind:     hidden_remainder_y
      - .offset:         94
        .size:           2
        .value_kind:     hidden_remainder_z
      - .offset:         112
        .size:           8
        .value_kind:     hidden_global_offset_x
      - .offset:         120
        .size:           8
        .value_kind:     hidden_global_offset_y
      - .offset:         128
        .size:           8
        .value_kind:     hidden_global_offset_z
      - .offset:         136
        .size:           2
        .value_kind:     hidden_grid_dims
      - .offset:         192
        .size:           4
        .value_kind:     hidden_dynamic_lds_size
    .group_segment_fixed_size: 0
    .kernarg_segment_align: 8
    .kernarg_segment_size: 328
    .language:       OpenCL C
    .language_version:
      - 2
      - 0
    .max_flat_workgroup_size: 512
    .name:           _Z9gemm_fastILi2ELi2EEvPKtS1_iiii7EpiArgs
    .private_segment_fixed_size: 0
    .sgpr_count:     53
    .sgpr_spill_count: 0
    .symbol:         _Z9gemm_fastILi2ELi2EEvPKtS1_iiii7EpiArgs.kd
    .uniform_work_group_size: 1
    .uses_dynamic_stack: false
    .vgpr_count:     248
    .vgpr_spill_count: 0
    .wavefront_size: 64
  - .agpr_count:     0
    .args:
      - .actual_access:  read_only
        .address_space:  global
        .offset:         0
        .size:           8
        .value_kind:     global_buffer
      - .actual_access:  read_only
        .address_space:  global
        .offset:         8
        .size:           8
        .value_kind:     global_buffer
      - .actual_access:  read_only
        .address_space:  global
        .offset:         16
        .size:           8
        .value_kind:     global_buffer
      - .actual_access:  read_only
        .address_space:  global
        .offset:         24
        .size:           8
        .value_kind:     global_buffer
      - .actual_access:  write_only
        .address_space:  global
        .offset:         32
        .size:           8
        .value_kind:     global_buffer
      - .actual_access:  write_only
        .address_space:  global
        .offset:         40
        .size:           8
        .value_kind:     global_buffer
      - .actual_access:  read_only
        .address_space:  global
        .offset:         48
        .size:           8
        .value_kind:     global_buffer
      - .actual_access:  read_only
        .address_space:  global
        .offset:         56
        .size:           8
        .value_kind:     global_buffer
    .group_segment_fixed_size: 16
    .kernarg_segment_align: 8
    .kernarg_segment_size: 64
    .language:       OpenCL C
    .language_version:
      - 2
      - 0
    .max_flat_workgroup_size: 256
    .name:           _Z9ln_kernelILb1ELb0EEvPKvPKtS3_PKfPvPtS5_S5_
    .private_segment_fixed_size: 0
    .sgpr_count:     34
    .sgpr_spill_count: 0
    .symbol:         _Z9ln_kernelILb1ELb0EEvPKvPKtS3_PKfPvPtS5_S5_.kd
    .uniform_work_group_size: 1
    .uses_dynamic_stack: false
    .vgpr_count:     62
    .vgpr_spill_count: 0
    .wavefront_size: 64
